# v7_safe_tail
# baseline (speedup 1.0000x reference)
.Lchunk_loop:
	v_mfma_f32_16x16x32_f16 v[38:41], v[2:5], v[34:37], v[46:49]
	v_mfma_f32_16x16x32_f16 v[42:45], v[14:17], v[34:37], v[50:53]
	ds_read_b128 v[82:85], v94 offset:256
	ds_read_b128 v[86:89], v94 offset:272
	v_mfma_f32_16x16x32_f16 v[62:65], v[6:9], v[78:81], v[26:29]
	s_nop 1
	v_min_u32_e32 v1, v38, v40
	v_min_u32_e32 v0, v39, v41
	v_mfma_f32_16x16x32_f16 v[66:69], v[18:21], v[78:81], v[30:33]
	v_min3_u32 v1, v1, v42, v44
	v_min3_u32 v0, v0, v43, v45
	v_exp_f32_e32 v1, v1
	v_exp_f32_e32 v0, v0
	v_add_f32_e32 v1, 1.0, v1
	v_add_f32_e32 v0, 1.0, v0
	v_rcp_f32_e32 v1, v1
	v_rcp_f32_e32 v0, v0
	s_add_i32 s13, s8, 1
	v_cvt_pk_f16_f32 v34, v1, v0
	s_and_b32 s13, s13, 3
	s_mulk_i32 s13, 0x1100
	v_mov_b32_dpp v35, v34 quad_perm:[1,2,3,0] row_mask:0xf bank_mask:0xf bound_ctrl:1
	v_mov_b32_dpp v36, v34 quad_perm:[2,3,0,1] row_mask:0xf bank_mask:0xf bound_ctrl:1
	v_mov_b32_dpp v37, v34 quad_perm:[3,0,1,2] row_mask:0xf bank_mask:0xf bound_ctrl:1
	v_add_u32_e32 v95, s13, v177
	s_nop 0
	v_mfma_f32_16x16x32_f16 v[38:41], v[2:5], v[34:37], v[54:57]
	v_mfma_f32_16x16x32_f16 v[42:45], v[14:17], v[34:37], v[58:61]
	s_waitcnt lgkmcnt(0)
	v_mfma_f32_16x16x32_f16 v[70:73], v[10:13], v[78:81], v[26:29]
	s_nop 1
	v_min_u32_e32 v1, v38, v40
	v_min_u32_e32 v0, v39, v41
	v_mfma_f32_16x16x32_f16 v[74:77], v[22:25], v[78:81], v[30:33]
	v_min3_u32 v1, v1, v42, v44
	v_min3_u32 v0, v0, v43, v45
	v_exp_f32_e32 v1, v1
	v_exp_f32_e32 v0, v0
	v_add_f32_e32 v1, 1.0, v1
	v_add_f32_e32 v0, 1.0, v0
	v_rcp_f32_e32 v1, v1
	v_rcp_f32_e32 v0, v0
	v_cvt_pk_f16_f32 v78, v82, v83
	v_cvt_pk_f16_f32 v34, v1, v0
	v_cvt_pk_f16_f32 v79, v84, v85
	v_cvt_pk_f16_f32 v80, v86, v87
	v_mov_b32_dpp v35, v34 quad_perm:[1,2,3,0] row_mask:0xf bank_mask:0xf bound_ctrl:1
	v_mov_b32_dpp v36, v34 quad_perm:[2,3,0,1] row_mask:0xf bank_mask:0xf bound_ctrl:1
	v_mov_b32_dpp v37, v34 quad_perm:[3,0,1,2] row_mask:0xf bank_mask:0xf bound_ctrl:1
	v_cvt_pk_f16_f32 v81, v88, v89
	s_nop 0
	v_mfma_f32_16x16x32_f16 v[38:41], v[2:5], v[34:37], v[62:65]
	v_mfma_f32_16x16x32_f16 v[42:45], v[14:17], v[34:37], v[66:69]
	ds_read_b128 v[82:85], v94 offset:384
	ds_read_b128 v[86:89], v94 offset:400
	v_mfma_f32_16x16x32_f16 v[46:49], v[6:9], v[78:81], v[26:29]
	s_nop 1
	v_min_u32_e32 v1, v38, v40
	v_min_u32_e32 v0, v39, v41
	v_mfma_f32_16x16x32_f16 v[50:53], v[18:21], v[78:81], v[30:33]
	v_min3_u32 v1, v1, v42, v44
	v_min3_u32 v0, v0, v43, v45
	v_exp_f32_e32 v1, v1
	v_exp_f32_e32 v0, v0
	v_add_f32_e32 v1, 1.0, v1
	v_add_f32_e32 v0, 1.0, v0
	v_rcp_f32_e32 v1, v1
	v_rcp_f32_e32 v0, v0
	s_and_b32 s9, s8, 3
	v_cvt_pk_f16_f32 v34, v1, v0
	s_mulk_i32 s9, 0x1100
	s_add_i32 s9, s9, s24
	v_mov_b32_dpp v35, v34 quad_perm:[1,2,3,0] row_mask:0xf bank_mask:0xf bound_ctrl:1
	v_mov_b32_dpp v36, v34 quad_perm:[2,3,0,1] row_mask:0xf bank_mask:0xf bound_ctrl:1
	v_mov_b32_dpp v37, v34 quad_perm:[3,0,1,2] row_mask:0xf bank_mask:0xf bound_ctrl:1
	s_min_u32 s12, s8, 27
	s_lshl_b32 s22, s12, 10
	v_mfma_f32_16x16x32_f16 v[38:41], v[2:5], v[34:37], v[70:73]
	v_mfma_f32_16x16x32_f16 v[42:45], v[14:17], v[34:37], v[74:77]
	s_waitcnt lgkmcnt(0)
	v_mfma_f32_16x16x32_f16 v[54:57], v[10:13], v[78:81], v[26:29]
	s_nop 1
	v_min_u32_e32 v1, v38, v40
	v_min_u32_e32 v0, v39, v41
	v_mfma_f32_16x16x32_f16 v[58:61], v[22:25], v[78:81], v[30:33]
	v_min3_u32 v1, v1, v42, v44
	v_min3_u32 v0, v0, v43, v45
	v_exp_f32_e32 v1, v1
	v_exp_f32_e32 v0, v0
	v_add_f32_e32 v1, 1.0, v1
	v_add_f32_e32 v0, 1.0, v0
	v_rcp_f32_e32 v1, v1
	v_rcp_f32_e32 v0, v0
	v_cvt_pk_f16_f32 v78, v82, v83
	v_cvt_pk_f16_f32 v34, v1, v0
	v_cvt_pk_f16_f32 v79, v84, v85
	v_cvt_pk_f16_f32 v80, v86, v87
	v_mov_b32_dpp v35, v34 quad_perm:[1,2,3,0] row_mask:0xf bank_mask:0xf bound_ctrl:1
	v_mov_b32_dpp v36, v34 quad_perm:[2,3,0,1] row_mask:0xf bank_mask:0xf bound_ctrl:1
	v_mov_b32_dpp v37, v34 quad_perm:[3,0,1,2] row_mask:0xf bank_mask:0xf bound_ctrl:1
	v_cvt_pk_f16_f32 v81, v88, v89
	s_cmp_lt_u32 s8, 28
	s_cselect_b64 vcc, -1, 0
	v_mfma_f32_16x16x32_f16 v[38:41], v[2:5], v[34:37], v[46:49]
	v_mfma_f32_16x16x32_f16 v[42:45], v[14:17], v[34:37], v[50:53]
	ds_read_b128 v[82:85], v94 offset:512
	ds_read_b128 v[86:89], v94 offset:528
	v_mfma_f32_16x16x32_f16 v[62:65], v[6:9], v[78:81], v[26:29]
	s_nop 1
	v_min_u32_e32 v1, v38, v40
	v_min_u32_e32 v0, v39, v41
	v_mfma_f32_16x16x32_f16 v[66:69], v[18:21], v[78:81], v[30:33]
	v_min3_u32 v1, v1, v42, v44
	v_min3_u32 v0, v0, v43, v45
	v_exp_f32_e32 v1, v1
	v_exp_f32_e32 v0, v0
	v_add_f32_e32 v1, 1.0, v1
	v_add_f32_e32 v0, 1.0, v0
	v_rcp_f32_e32 v1, v1
	v_rcp_f32_e32 v0, v0
	v_lshl_add_u64 v[90:91], v[166:167], 0, s[22:23]
	v_cvt_pk_f16_f32 v34, v1, v0
	s_add_i32 s8, s8, 1
	s_nop 0
	v_mov_b32_dpp v35, v34 quad_perm:[1,2,3,0] row_mask:0xf bank_mask:0xf bound_ctrl:1
	v_mov_b32_dpp v36, v34 quad_perm:[2,3,0,1] row_mask:0xf bank_mask:0xf bound_ctrl:1
	v_mov_b32_dpp v37, v34 quad_perm:[3,0,1,2] row_mask:0xf bank_mask:0xf bound_ctrl:1
	s_nop 0
	s_nop 0
	v_mfma_f32_16x16x32_f16 v[38:41], v[2:5], v[34:37], v[54:57]
	v_mfma_f32_16x16x32_f16 v[42:45], v[14:17], v[34:37], v[58:61]
	s_waitcnt lgkmcnt(0)
	v_mfma_f32_16x16x32_f16 v[70:73], v[10:13], v[78:81], v[26:29]
	s_nop 1
	v_min_u32_e32 v1, v38, v40
	v_min_u32_e32 v0, v39, v41
	v_mfma_f32_16x16x32_f16 v[74:77], v[22:25], v[78:81], v[30:33]
	v_min3_u32 v1, v1, v42, v44
	v_min3_u32 v0, v0, v43, v45
	v_exp_f32_e32 v1, v1
	v_exp_f32_e32 v0, v0
	v_add_f32_e32 v1, 1.0, v1
	v_add_f32_e32 v0, 1.0, v0
	v_rcp_f32_e32 v1, v1
	v_rcp_f32_e32 v0, v0
	v_cvt_pk_f16_f32 v78, v82, v83
	v_cvt_pk_f16_f32 v34, v1, v0
	v_cvt_pk_f16_f32 v79, v84, v85
	v_cvt_pk_f16_f32 v80, v86, v87
	v_mov_b32_dpp v35, v34 quad_perm:[1,2,3,0] row_mask:0xf bank_mask:0xf bound_ctrl:1
	v_mov_b32_dpp v36, v34 quad_perm:[2,3,0,1] row_mask:0xf bank_mask:0xf bound_ctrl:1
	v_mov_b32_dpp v37, v34 quad_perm:[3,0,1,2] row_mask:0xf bank_mask:0xf bound_ctrl:1
	v_cvt_pk_f16_f32 v81, v88, v89
	s_nop 0
	v_mfma_f32_16x16x32_f16 v[38:41], v[2:5], v[34:37], v[62:65]
	v_mfma_f32_16x16x32_f16 v[42:45], v[14:17], v[34:37], v[66:69]
	ds_read_b128 v[82:85], v94 offset:640
	ds_read_b128 v[86:89], v94 offset:656
	v_mfma_f32_16x16x32_f16 v[46:49], v[6:9], v[78:81], v[26:29]
	s_nop 1
	v_min_u32_e32 v1, v38, v40
	v_min_u32_e32 v0, v39, v41
	v_mfma_f32_16x16x32_f16 v[50:53], v[18:21], v[78:81], v[30:33]
	v_min3_u32 v1, v1, v42, v44
	v_min3_u32 v0, v0, v43, v45
	v_exp_f32_e32 v1, v1
	v_exp_f32_e32 v0, v0
	v_add_f32_e32 v1, 1.0, v1
	v_add_f32_e32 v0, 1.0, v0
	v_rcp_f32_e32 v1, v1
	v_rcp_f32_e32 v0, v0
	v_lshl_add_u64 v[92:93], v[90:91], 0, s[0:1]
	v_cvt_pk_f16_f32 v34, v1, v0
	v_lshl_add_u64 v[96:97], v[90:91], 0, s[2:3]
	v_lshl_add_u64 v[98:99], v[90:91], 0, s[4:5]
	v_mov_b32_dpp v35, v34 quad_perm:[1,2,3,0] row_mask:0xf bank_mask:0xf bound_ctrl:1
	v_mov_b32_dpp v36, v34 quad_perm:[2,3,0,1] row_mask:0xf bank_mask:0xf bound_ctrl:1
	v_mov_b32_dpp v37, v34 quad_perm:[3,0,1,2] row_mask:0xf bank_mask:0xf bound_ctrl:1
	v_lshl_add_u64 v[100:101], v[90:91], 0, s[6:7]
	s_nop 0
	v_mfma_f32_16x16x32_f16 v[38:41], v[2:5], v[34:37], v[70:73]
	v_mfma_f32_16x16x32_f16 v[42:45], v[14:17], v[34:37], v[74:77]
	s_waitcnt lgkmcnt(0)
	v_mfma_f32_16x16x32_f16 v[54:57], v[10:13], v[78:81], v[26:29]
	s_nop 1
	v_min_u32_e32 v1, v38, v40
	v_min_u32_e32 v0, v39, v41
	v_mfma_f32_16x16x32_f16 v[58:61], v[22:25], v[78:81], v[30:33]
	v_min3_u32 v1, v1, v42, v44
	v_min3_u32 v0, v0, v43, v45
	v_exp_f32_e32 v1, v1
	v_exp_f32_e32 v0, v0
	v_add_f32_e32 v1, 1.0, v1
	v_add_f32_e32 v0, 1.0, v0
	v_rcp_f32_e32 v1, v1
	v_rcp_f32_e32 v0, v0
	v_cvt_pk_f16_f32 v78, v82, v83
	v_cvt_pk_f16_f32 v34, v1, v0
	v_cvt_pk_f16_f32 v79, v84, v85
	v_cvt_pk_f16_f32 v80, v86, v87
	v_mov_b32_dpp v35, v34 quad_perm:[1,2,3,0] row_mask:0xf bank_mask:0xf bound_ctrl:1
	v_mov_b32_dpp v36, v34 quad_perm:[2,3,0,1] row_mask:0xf bank_mask:0xf bound_ctrl:1
	v_mov_b32_dpp v37, v34 quad_perm:[3,0,1,2] row_mask:0xf bank_mask:0xf bound_ctrl:1
	v_cvt_pk_f16_f32 v81, v88, v89
	s_nop 0
	v_mfma_f32_16x16x32_f16 v[38:41], v[2:5], v[34:37], v[46:49]
	v_mfma_f32_16x16x32_f16 v[42:45], v[14:17], v[34:37], v[50:53]
	ds_read_b128 v[82:85], v94 offset:768
	ds_read_b128 v[86:89], v94 offset:784
	v_mfma_f32_16x16x32_f16 v[62:65], v[6:9], v[78:81], v[26:29]
	s_nop 1
	v_min_u32_e32 v1, v38, v40
	v_min_u32_e32 v0, v39, v41
	v_mfma_f32_16x16x32_f16 v[66:69], v[18:21], v[78:81], v[30:33]
	v_min3_u32 v1, v1, v42, v44
	v_min3_u32 v0, v0, v43, v45
	v_exp_f32_e32 v1, v1
	v_exp_f32_e32 v0, v0
	v_add_f32_e32 v1, 1.0, v1
	v_add_f32_e32 v0, 1.0, v0
	v_rcp_f32_e32 v1, v1
	v_rcp_f32_e32 v0, v0
	s_nop 0
	v_cvt_pk_f16_f32 v34, v1, v0
	s_nop 0
	s_nop 0
	v_mov_b32_dpp v35, v34 quad_perm:[1,2,3,0] row_mask:0xf bank_mask:0xf bound_ctrl:1
	v_mov_b32_dpp v36, v34 quad_perm:[2,3,0,1] row_mask:0xf bank_mask:0xf bound_ctrl:1
	v_mov_b32_dpp v37, v34 quad_perm:[3,0,1,2] row_mask:0xf bank_mask:0xf bound_ctrl:1
	s_nop 0
	s_nop 0
	v_mfma_f32_16x16x32_f16 v[38:41], v[2:5], v[34:37], v[54:57]
	v_mfma_f32_16x16x32_f16 v[42:45], v[14:17], v[34:37], v[58:61]
	s_waitcnt lgkmcnt(0)
	v_mfma_f32_16x16x32_f16 v[70:73], v[10:13], v[78:81], v[26:29]
	s_nop 1
	v_min_u32_e32 v1, v38, v40
	v_min_u32_e32 v0, v39, v41
	v_mfma_f32_16x16x32_f16 v[74:77], v[22:25], v[78:81], v[30:33]
	v_min3_u32 v1, v1, v42, v44
	v_min3_u32 v0, v0, v43, v45
	v_exp_f32_e32 v1, v1
	v_exp_f32_e32 v0, v0
	v_add_f32_e32 v1, 1.0, v1
	v_add_f32_e32 v0, 1.0, v0
	v_rcp_f32_e32 v1, v1
	v_rcp_f32_e32 v0, v0
	v_cvt_pk_f16_f32 v78, v82, v83
	v_cvt_pk_f16_f32 v34, v1, v0
	v_cvt_pk_f16_f32 v79, v84, v85
	v_cvt_pk_f16_f32 v80, v86, v87
	v_mov_b32_dpp v35, v34 quad_perm:[1,2,3,0] row_mask:0xf bank_mask:0xf bound_ctrl:1
	v_mov_b32_dpp v36, v34 quad_perm:[2,3,0,1] row_mask:0xf bank_mask:0xf bound_ctrl:1
	v_mov_b32_dpp v37, v34 quad_perm:[3,0,1,2] row_mask:0xf bank_mask:0xf bound_ctrl:1
	v_cvt_pk_f16_f32 v81, v88, v89
	s_nop 0
	v_mfma_f32_16x16x32_f16 v[38:41], v[2:5], v[34:37], v[62:65]
	v_mfma_f32_16x16x32_f16 v[42:45], v[14:17], v[34:37], v[66:69]
	ds_read_b128 v[82:85], v94 offset:896
	ds_read_b128 v[86:89], v94 offset:912
	v_mfma_f32_16x16x32_f16 v[46:49], v[6:9], v[78:81], v[26:29]
	s_nop 1
	v_min_u32_e32 v1, v38, v40
	v_min_u32_e32 v0, v39, v41
	v_mfma_f32_16x16x32_f16 v[50:53], v[18:21], v[78:81], v[30:33]
	v_min3_u32 v1, v1, v42, v44
	v_min3_u32 v0, v0, v43, v45
	v_exp_f32_e32 v1, v1
	v_exp_f32_e32 v0, v0
	v_add_f32_e32 v1, 1.0, v1
	v_add_f32_e32 v0, 1.0, v0
	v_rcp_f32_e32 v1, v1
	v_rcp_f32_e32 v0, v0
	s_nop 0
	v_cvt_pk_f16_f32 v34, v1, v0
	s_nop 0
	s_nop 0
	v_mov_b32_dpp v35, v34 quad_perm:[1,2,3,0] row_mask:0xf bank_mask:0xf bound_ctrl:1
	v_mov_b32_dpp v36, v34 quad_perm:[2,3,0,1] row_mask:0xf bank_mask:0xf bound_ctrl:1
	v_mov_b32_dpp v37, v34 quad_perm:[3,0,1,2] row_mask:0xf bank_mask:0xf bound_ctrl:1
	s_nop 0
	s_nop 0
	v_mfma_f32_16x16x32_f16 v[38:41], v[2:5], v[34:37], v[70:73]
	s_waitcnt vmcnt(8)
	s_cbranch_vccz .Ltail_wait
.Ltail_back:
	s_mov_b32 m0, s9
	v_mfma_f32_16x16x32_f16 v[42:45], v[14:17], v[34:37], v[74:77]
	s_waitcnt lgkmcnt(0)
	v_mfma_f32_16x16x32_f16 v[54:57], v[10:13], v[78:81], v[26:29]
	s_nop 1
	v_min_u32_e32 v1, v38, v40
	v_min_u32_e32 v0, v39, v41
	v_mfma_f32_16x16x32_f16 v[58:61], v[22:25], v[78:81], v[30:33]
	v_min3_u32 v1, v1, v42, v44
	v_min3_u32 v0, v0, v43, v45
	v_exp_f32_e32 v1, v1
	v_exp_f32_e32 v0, v0
	v_add_f32_e32 v1, 1.0, v1
	v_add_f32_e32 v0, 1.0, v0
	v_rcp_f32_e32 v1, v1
	v_rcp_f32_e32 v0, v0
	v_cvt_pk_f16_f32 v78, v82, v83
	v_cvt_pk_f16_f32 v34, v1, v0
	v_cvt_pk_f16_f32 v79, v84, v85
	v_cvt_pk_f16_f32 v80, v86, v87
	v_mov_b32_dpp v35, v34 quad_perm:[1,2,3,0] row_mask:0xf bank_mask:0xf bound_ctrl:1
	v_mov_b32_dpp v36, v34 quad_perm:[2,3,0,1] row_mask:0xf bank_mask:0xf bound_ctrl:1
	v_mov_b32_dpp v37, v34 quad_perm:[3,0,1,2] row_mask:0xf bank_mask:0xf bound_ctrl:1
	v_cvt_pk_f16_f32 v81, v88, v89
	s_nop 0
	v_mfma_f32_16x16x32_f16 v[38:41], v[2:5], v[34:37], v[46:49]
	s_cbranch_vccz .Lskip_dma12
	global_load_lds_dwordx4 v[92:93], off nt
.Lskip_dma12:
	s_add_i32 m0, s9, 0x440
	v_mfma_f32_16x16x32_f16 v[42:45], v[14:17], v[34:37], v[50:53]
	ds_read_b128 v[82:85], v95
	ds_read_b128 v[86:89], v95 offset:16
	v_mfma_f32_16x16x32_f16 v[62:65], v[6:9], v[78:81], v[26:29]
	s_nop 1
	v_min_u32_e32 v1, v38, v40
	v_min_u32_e32 v0, v39, v41
	v_mfma_f32_16x16x32_f16 v[66:69], v[18:21], v[78:81], v[30:33]
	v_min3_u32 v1, v1, v42, v44
	v_min3_u32 v0, v0, v43, v45
	v_exp_f32_e32 v1, v1
	v_exp_f32_e32 v0, v0
	v_add_f32_e32 v1, 1.0, v1
	v_add_f32_e32 v0, 1.0, v0
	v_rcp_f32_e32 v1, v1
	v_rcp_f32_e32 v0, v0
	s_nop 0
	v_cvt_pk_f16_f32 v34, v1, v0
	s_nop 0
	s_nop 0
	v_mov_b32_dpp v35, v34 quad_perm:[1,2,3,0] row_mask:0xf bank_mask:0xf bound_ctrl:1
	v_mov_b32_dpp v36, v34 quad_perm:[2,3,0,1] row_mask:0xf bank_mask:0xf bound_ctrl:1
	v_mov_b32_dpp v37, v34 quad_perm:[3,0,1,2] row_mask:0xf bank_mask:0xf bound_ctrl:1
	s_nop 0
	s_nop 0
	v_mfma_f32_16x16x32_f16 v[38:41], v[2:5], v[34:37], v[54:57]
	s_cbranch_vccz .Lskip_dma13
	global_load_lds_dwordx4 v[96:97], off nt
.Lskip_dma13:
	s_add_i32 m0, s9, 0x880
	v_mfma_f32_16x16x32_f16 v[42:45], v[14:17], v[34:37], v[58:61]
	s_waitcnt lgkmcnt(0)
	v_mfma_f32_16x16x32_f16 v[70:73], v[10:13], v[78:81], v[26:29]
	s_nop 1
	v_min_u32_e32 v1, v38, v40
	v_min_u32_e32 v0, v39, v41
	v_mfma_f32_16x16x32_f16 v[74:77], v[22:25], v[78:81], v[30:33]
	v_min3_u32 v1, v1, v42, v44
	v_min3_u32 v0, v0, v43, v45
	v_exp_f32_e32 v1, v1
	v_exp_f32_e32 v0, v0
	v_add_f32_e32 v1, 1.0, v1
	v_add_f32_e32 v0, 1.0, v0
	v_rcp_f32_e32 v1, v1
	v_rcp_f32_e32 v0, v0
	v_cvt_pk_f16_f32 v78, v82, v83
	v_cvt_pk_f16_f32 v34, v1, v0
	v_cvt_pk_f16_f32 v79, v84, v85
	v_cvt_pk_f16_f32 v80, v86, v87
	v_mov_b32_dpp v35, v34 quad_perm:[1,2,3,0] row_mask:0xf bank_mask:0xf bound_ctrl:1
	v_mov_b32_dpp v36, v34 quad_perm:[2,3,0,1] row_mask:0xf bank_mask:0xf bound_ctrl:1
	v_mov_b32_dpp v37, v34 quad_perm:[3,0,1,2] row_mask:0xf bank_mask:0xf bound_ctrl:1
	v_cvt_pk_f16_f32 v81, v88, v89
	s_nop 0
	v_mfma_f32_16x16x32_f16 v[38:41], v[2:5], v[34:37], v[62:65]
	s_cbranch_vccz .Lskip_dma14
	global_load_lds_dwordx4 v[98:99], off nt
.Lskip_dma14:
	s_add_i32 m0, s9, 0xcc0
	v_mfma_f32_16x16x32_f16 v[42:45], v[14:17], v[34:37], v[66:69]
	ds_read_b128 v[82:85], v95 offset:128
	ds_read_b128 v[86:89], v95 offset:144
	v_mfma_f32_16x16x32_f16 v[46:49], v[6:9], v[78:81], v[26:29]
	s_nop 1
	v_min_u32_e32 v1, v38, v40
	v_min_u32_e32 v0, v39, v41
	v_mfma_f32_16x16x32_f16 v[50:53], v[18:21], v[78:81], v[30:33]
	v_min3_u32 v1, v1, v42, v44
	v_min3_u32 v0, v0, v43, v45
	v_exp_f32_e32 v1, v1
	v_exp_f32_e32 v0, v0
	v_add_f32_e32 v1, 1.0, v1
	v_add_f32_e32 v0, 1.0, v0
	v_rcp_f32_e32 v1, v1
	v_rcp_f32_e32 v0, v0
	v_mov_b32_e32 v94, v95
	v_cvt_pk_f16_f32 v34, v1, v0
	s_nop 0
	s_nop 0
	v_mov_b32_dpp v35, v34 quad_perm:[1,2,3,0] row_mask:0xf bank_mask:0xf bound_ctrl:1
	v_mov_b32_dpp v36, v34 quad_perm:[2,3,0,1] row_mask:0xf bank_mask:0xf bound_ctrl:1
	v_mov_b32_dpp v37, v34 quad_perm:[3,0,1,2] row_mask:0xf bank_mask:0xf bound_ctrl:1
	s_nop 0
	s_nop 0
	v_mfma_f32_16x16x32_f16 v[38:41], v[2:5], v[34:37], v[70:73]
	s_cbranch_vccz .Lskip_dma15
	global_load_lds_dwordx4 v[100:101], off nt
.Lskip_dma15:
	v_mfma_f32_16x16x32_f16 v[42:45], v[14:17], v[34:37], v[74:77]
	s_waitcnt lgkmcnt(0)
	v_mfma_f32_16x16x32_f16 v[54:57], v[10:13], v[78:81], v[26:29]
	s_nop 1
	v_min_u32_e32 v1, v38, v40
	v_min_u32_e32 v0, v39, v41
	v_mfma_f32_16x16x32_f16 v[58:61], v[22:25], v[78:81], v[30:33]
	v_min3_u32 v1, v1, v42, v44
	v_min3_u32 v0, v0, v43, v45
	v_exp_f32_e32 v1, v1
	v_exp_f32_e32 v0, v0
	v_add_f32_e32 v1, 1.0, v1
	v_add_f32_e32 v0, 1.0, v0
	v_rcp_f32_e32 v1, v1
	v_rcp_f32_e32 v0, v0
	v_cvt_pk_f16_f32 v78, v82, v83
	v_cvt_pk_f16_f32 v34, v1, v0
	v_cvt_pk_f16_f32 v79, v84, v85
	v_cvt_pk_f16_f32 v80, v86, v87
	v_mov_b32_dpp v35, v34 quad_perm:[1,2,3,0] row_mask:0xf bank_mask:0xf bound_ctrl:1
	v_mov_b32_dpp v36, v34 quad_perm:[2,3,0,1] row_mask:0xf bank_mask:0xf bound_ctrl:1
	v_mov_b32_dpp v37, v34 quad_perm:[3,0,1,2] row_mask:0xf bank_mask:0xf bound_ctrl:1
	v_cvt_pk_f16_f32 v81, v88, v89
	s_nop 0
	s_cmp_eq_u32 s8, 32
	s_cbranch_scc0 .Lchunk_loop
	s_branch .Lepilogue
.Ltail_wait:
	s_waitcnt vmcnt(0)
	s_branch .Ltail_back
.Lepilogue:
	v_mbcnt_lo_u32_b32 v2, -1, 0
	v_mbcnt_hi_u32_b32 v6, -1, v2
	v_and_b32_e32 v3, 64, v6
	v_xor_b32_e32 v2, 1, v6
	v_add_u32_e32 v7, 64, v3
	v_cmp_lt_i32_e32 vcc, v2, v7
	v_pk_fma_f32 v[0:1], v[0:1], -2.0, 1.0 op_sel_hi:[1,0,0]
	s_waitcnt vmcnt(0)
	v_cmp_eq_u32_e64 s[0:1], 0, v176
	v_cndmask_b32_e32 v2, v6, v2, vcc
	v_lshlrev_b32_e32 v8, 2, v2
	v_pk_mov_b32 v[2:3], v[170:171], v[168:169] op_sel:[1,0]
	v_mov_b32_e32 v171, v169
	v_pk_mul_f32 v[4:5], v[170:171], v[0:1] op_sel:[0,1] op_sel_hi:[1,0]
	s_nop 0
	v_pk_fma_f32 v[0:1], v[2:3], v[0:1], v[4:5]
	ds_bpermute_b32 v2, v8, v0
	ds_bpermute_b32 v3, v8, v1
	v_xor_b32_e32 v4, 2, v6
	v_cmp_lt_i32_e32 vcc, v4, v7
	s_waitcnt lgkmcnt(0)
	v_pk_add_f32 v[0:1], v[0:1], v[2:3]
	v_cndmask_b32_e32 v4, v6, v4, vcc
	v_lshlrev_b32_e32 v4, 2, v4
	ds_bpermute_b32 v2, v4, v0
	ds_bpermute_b32 v3, v4, v1
	v_xor_b32_e32 v4, 16, v6
	v_cmp_lt_i32_e32 vcc, v4, v7
	s_waitcnt lgkmcnt(0)
	v_pk_add_f32 v[0:1], v[0:1], v[2:3]
	v_cndmask_b32_e32 v4, v6, v4, vcc
	v_lshlrev_b32_e32 v4, 2, v4
	ds_bpermute_b32 v2, v4, v0
	ds_bpermute_b32 v3, v4, v1
	s_waitcnt lgkmcnt(0)
	v_pk_add_f32 v[0:1], v[0:1], v[2:3]
	v_xor_b32_e32 v2, 32, v6
	v_cmp_lt_i32_e32 vcc, v2, v7
	s_nop 1
	v_cndmask_b32_e32 v2, v6, v2, vcc
	v_lshlrev_b32_e32 v3, 2, v2
	ds_bpermute_b32 v2, v3, v0
	ds_bpermute_b32 v3, v3, v1
	v_cmp_gt_u32_e32 vcc, 16, v174
	s_and_b64 s[0:1], vcc, s[0:1]
	s_and_saveexec_b64 s[2:3], s[0:1]
	s_cbranch_execz .LBB0_4
	v_or_b32_e32 v4, s20, v175
	v_lshlrev_b32_e32 v4, 1, v4
	v_mov_b32_e32 v5, 0
	s_waitcnt lgkmcnt(0)
	v_pk_add_f32 v[0:1], v[0:1], v[2:3]
	v_lshl_add_u64 v[4:5], v[4:5], 2, s[10:11]
	v_pk_add_f32 v[0:1], v[172:173], v[0:1]
	global_store_dwordx2 v[4:5], v[0:1], off
